# v21 plus first KV tile DMA of each pass issued at the top of the q prologue
# baseline (speedup 1.0000x reference)
; __device__ __forceinline__ float bf2f(unsigned b) { return __uint_as_float(b << 16); }
; __device__ __forceinline__ float rsq(float x) { return __builtin_amdgcn_rsqf(x); }
; template <int layer>
; __device__ __forceinline__ void attn_phase(LAS unsigned char* lds) {
;     ...
;             {
;                 const size_t tq = (size_t)b * SEQ + qlo + r32;
;                 const bf16* qp = Qs + tq * QLD + h * QHS + hi * 8;
;                 u32x4 raw[NQ];
; #pragma unroll
;                 for (int d0 = 0; d0 < NQ; ++d0) raw[d0] = *(const u32x4*)(qp + d0 * 16);
;                 float ss = 0.f;
; #pragma unroll
;                 for (int d0 = 0; d0 < 8; ++d0)
; #pragma unroll
;                     for (int j = 0; j < 4; ++j) { const float x0 = bf2f(raw[d0][j] & 0xffffu), x1 = bf2f(raw[d0][j] >> 16); ss += x0 * x0 + x1 * x1; }
;                 { auto rr = __builtin_amdgcn_permlane32_swap(__float_as_uint(ss), __float_as_uint(ss), false, false); ss = __uint_as_float(rr[0]) + __uint_as_float(rr[1]); }
;                 const float rn = rsq(ss * (1.0f / 128) + EPS) * C2;
.LBB0_529:
	s_andn2_b64 vcc, exec, s[18:19]
	s_cbranch_vccnz .Lskip_issue0_a0
	s_mov_b32 m0, s65
	s_nop 0
	global_load_lds_dwordx4 v1, s[34:35]
	s_mov_b32 m0, s73
	s_nop 0
	global_load_lds_dwordx4 v208, s[34:35]
	s_mov_b32 m0, s74
	s_nop 0
	global_load_lds_dwordx4 v209, s[34:35]
	s_mov_b32 m0, s75
	s_nop 0
	global_load_lds_dwordx4 v210, s[34:35]
	s_mov_b32 m0, s66
	s_nop 0
	global_load_lds_dwordx4 v188, s[38:39]
	s_mov_b32 m0, s76
	s_nop 0
	global_load_lds_dwordx4 v211, s[38:39]
	s_mov_b32 m0, s67
	s_nop 0
	global_load_lds_dwordx4 v181, s[36:37]
	s_mov_b32 m0, s64
	s_nop 0
	global_load_lds_dwordx4 v212, s[36:37]
	s_mov_b32 m0, s77
	s_nop 0
	global_load_lds_dwordx4 v213, s[36:37]
	s_mov_b32 m0, s78
	s_nop 0
	global_load_lds_dwordx4 v214, s[36:37]
.Lskip_issue0_a0:
	s_and_b64 s[4:5], s[6:7], exec
	v_readlane_b32 s4, v252, 26
	v_readlane_b32 s5, v252, 28
	s_cselect_b32 s8, s5, s4
	v_readlane_b32 s4, v252, 23
	s_add_i32 s28, s8, s4
	s_ashr_i32 s4, s28, 31
	s_add_u32 s14, s24, s28
	s_addc_u32 s60, s25, s4
	v_or_b32_e32 v28, s14, v180
	s_movk_i32 s4, 0x1800
	v_mad_u64_u32 v[20:21], s[4:5], v28, s4, v[186:187]
	v_mad_i32_i24 v21, s60, v217, v21
	global_load_dwordx4 v[22:25], v[20:21], off
	global_load_dwordx4 v[30:33], v[20:21], off offset:32
	global_load_dwordx4 v[34:37], v[20:21], off offset:64
	global_load_dwordx4 v[38:41], v[20:21], off offset:96
	global_load_dwordx4 v[16:19], v[20:21], off offset:128
	global_load_dwordx4 v[12:15], v[20:21], off offset:160
	global_load_dwordx4 v[8:11], v[20:21], off offset:192
	global_load_dwordx4 v[4:7], v[20:21], off offset:224
	v_readlane_b32 s16, v252, 19
	v_readlane_b32 s17, v252, 20
	s_andn2_b64 vcc, exec, s[18:19]
	s_waitcnt vmcnt(7)
	v_and_b32_e32 v27, 0xffff0000, v22
	v_and_b32_e32 v42, 0xffff0000, v23
	v_lshlrev_b32_e32 v26, 16, v22
	v_lshlrev_b32_e32 v29, 16, v23
	v_and_b32_e32 v44, 0xffff0000, v24
	s_waitcnt vmcnt(3)
	v_lshlrev_b32_e32 v71, 16, v16
	v_and_b32_e32 v72, 0xffff0000, v16
	v_mul_f32_e32 v2, v27, v27
	v_mul_f32_e32 v16, v42, v42
	v_lshlrev_b32_e32 v43, 16, v24
	v_and_b32_e32 v46, 0xffff0000, v25
	v_lshlrev_b32_e32 v73, 16, v17
	v_and_b32_e32 v74, 0xffff0000, v17
	v_mul_f32_e32 v17, v44, v44
	v_fmac_f32_e32 v2, v26, v26
	v_fmac_f32_e32 v16, v29, v29
	v_lshlrev_b32_e32 v45, 16, v25
	v_and_b32_e32 v48, 0xffff0000, v30
	v_mul_f32_e32 v22, v46, v46
	v_fmac_f32_e32 v17, v43, v43
	v_add_f32_e32 v2, v2, v16
	v_lshlrev_b32_e32 v47, 16, v30
	v_and_b32_e32 v50, 0xffff0000, v31
	v_mul_f32_e32 v23, v48, v48
	v_fmac_f32_e32 v22, v45, v45
	v_add_f32_e32 v2, v17, v2
	v_lshlrev_b32_e32 v49, 16, v31
	v_and_b32_e32 v52, 0xffff0000, v32
	v_mul_f32_e32 v24, v50, v50
	v_fmac_f32_e32 v23, v47, v47
	v_add_f32_e32 v2, v22, v2
	v_lshlrev_b32_e32 v51, 16, v32
	v_and_b32_e32 v54, 0xffff0000, v33
	v_mul_f32_e32 v25, v52, v52
	v_fmac_f32_e32 v24, v49, v49
	v_add_f32_e32 v2, v23, v2
	v_lshlrev_b32_e32 v53, 16, v33
	v_and_b32_e32 v56, 0xffff0000, v34
	v_mul_f32_e32 v30, v54, v54
	v_fmac_f32_e32 v25, v51, v51
	v_add_f32_e32 v2, v24, v2
	v_lshlrev_b32_e32 v55, 16, v34
	v_and_b32_e32 v58, 0xffff0000, v35
	v_mul_f32_e32 v31, v56, v56
	v_fmac_f32_e32 v30, v53, v53
	v_add_f32_e32 v2, v25, v2
	v_lshlrev_b32_e32 v57, 16, v35
	v_and_b32_e32 v60, 0xffff0000, v36
	v_mul_f32_e32 v32, v58, v58
	v_fmac_f32_e32 v31, v55, v55
	v_add_f32_e32 v2, v30, v2
	v_lshlrev_b32_e32 v59, 16, v36
	v_and_b32_e32 v62, 0xffff0000, v37
	v_mul_f32_e32 v33, v60, v60
	v_fmac_f32_e32 v32, v57, v57
	v_add_f32_e32 v2, v31, v2
	v_lshlrev_b32_e32 v61, 16, v37
	v_and_b32_e32 v64, 0xffff0000, v38
	v_mul_f32_e32 v34, v62, v62
	v_fmac_f32_e32 v33, v59, v59
	v_add_f32_e32 v2, v32, v2
	v_lshlrev_b32_e32 v63, 16, v38
	v_and_b32_e32 v66, 0xffff0000, v39
	v_mul_f32_e32 v35, v64, v64
	v_fmac_f32_e32 v34, v61, v61
	v_add_f32_e32 v2, v33, v2
	v_lshlrev_b32_e32 v65, 16, v39
	v_and_b32_e32 v68, 0xffff0000, v40
	v_mul_f32_e32 v36, v66, v66
	v_fmac_f32_e32 v35, v63, v63
	v_add_f32_e32 v2, v34, v2
	v_lshlrev_b32_e32 v67, 16, v40
	v_and_b32_e32 v70, 0xffff0000, v41
	v_mul_f32_e32 v37, v68, v68
	v_fmac_f32_e32 v36, v65, v65
	v_add_f32_e32 v2, v35, v2
	v_lshlrev_b32_e32 v69, 16, v41
	v_mul_f32_e32 v38, v70, v70
	v_fmac_f32_e32 v37, v67, v67
	v_add_f32_e32 v2, v36, v2
	v_mul_f32_e32 v39, v72, v72
	v_fmac_f32_e32 v38, v69, v69
	v_add_f32_e32 v2, v37, v2
	v_mul_f32_e32 v40, v74, v74
	v_fmac_f32_e32 v39, v71, v71
	v_add_f32_e32 v2, v38, v2
	v_fmac_f32_e32 v40, v73, v73
	v_add_f32_e32 v2, v39, v2
	v_add_f32_e32 v2, v40, v2
	global_load_dwordx4 v[22:25], v[184:185], off offset:16
	global_load_dwordx4 v[38:41], v[184:185], off
	v_and_b32_e32 v76, 0xffff0000, v18
	v_lshlrev_b32_e32 v75, 16, v18
	v_mul_f32_e32 v16, v76, v76
	v_fmac_f32_e32 v16, v75, v75
	v_and_b32_e32 v78, 0xffff0000, v19
	v_add_f32_e32 v2, v16, v2
	v_lshlrev_b32_e32 v77, 16, v19
	v_mul_f32_e32 v16, v78, v78
	s_waitcnt vmcnt(4)
	v_and_b32_e32 v80, 0xffff0000, v12
	v_fmac_f32_e32 v16, v77, v77
	v_lshlrev_b32_e32 v79, 16, v12
	v_mul_f32_e32 v12, v80, v80
	v_add_f32_e32 v2, v16, v2
	v_fmac_f32_e32 v12, v79, v79
	v_and_b32_e32 v82, 0xffff0000, v13
	v_add_f32_e32 v2, v12, v2
	v_lshlrev_b32_e32 v81, 16, v13
	v_mul_f32_e32 v12, v82, v82
	v_fmac_f32_e32 v12, v81, v81
	v_and_b32_e32 v84, 0xffff0000, v14
	v_add_f32_e32 v2, v12, v2
	v_lshlrev_b32_e32 v83, 16, v14
	v_mul_f32_e32 v12, v84, v84
	v_fmac_f32_e32 v12, v83, v83
	v_and_b32_e32 v86, 0xffff0000, v15
	v_add_f32_e32 v2, v12, v2
	v_lshlrev_b32_e32 v85, 16, v15
	v_mul_f32_e32 v12, v86, v86
	s_waitcnt vmcnt(3)
; __device__ __forceinline__ float bf2f(unsigned b) { return __uint_as_float(b << 16); }
; __device__ __forceinline__ float rsq(float x) { return __builtin_amdgcn_rsqf(x); }
; __device__ __forceinline__ unsigned cvtpk(float lo, float hi) { unsigned r; asm volatile("v_cvt_pk_bf16_f32 %0, %1, %2" : "=v"(r) : "v"(lo), "v"(hi)); return r; }
; template <int layer>
; __device__ __forceinline__ void attn_phase(LAS unsigned char* lds) {
;     ...
;                 float ss = 0.f;
; #pragma unroll
;                 for (int d0 = 0; d0 < 8; ++d0)
; #pragma unroll
;                     for (int j = 0; j < 4; ++j) { const float x0 = bf2f(raw[d0][j] & 0xffffu), x1 = bf2f(raw[d0][j] >> 16); ss += x0 * x0 + x1 * x1; }
;                 { auto rr = __builtin_amdgcn_permlane32_swap(__float_as_uint(ss), __float_as_uint(ss), false, false); ss = __uint_as_float(rr[0]) + __uint_as_float(rr[1]); }
;                 const float rn = rsq(ss * (1.0f / 128) + EPS) * C2;
; #pragma unroll
;                 for (int d0 = 0; d0 < 8; ++d0) { const f32x4 g0 = *(const f32x4*)(qkg + d0 * 16 + hi * 8), g1 = *(const f32x4*)(qkg + d0 * 16 + hi * 8 + 4); u32x4 o;
; #pragma unroll
;                     for (int j = 0; j < 4; ++j) { const float x0 = bf2f(raw[d0][j] & 0xffffu), x1 = bf2f(raw[d0][j] >> 16); const f32x4 gg = j < 2 ? g0 : g1;
;                         o[j] = cvtpk(x0 * rn * gg[(2 * j) & 3], x1 * rn * gg[(2 * j + 1) & 3]); }
;                     qr[d0] = *reinterpret_cast<bf16x8*>(&o); }
	v_and_b32_e32 v88, 0xffff0000, v8
	v_fmac_f32_e32 v12, v85, v85
	v_lshlrev_b32_e32 v87, 16, v8
	v_mul_f32_e32 v8, v88, v88
	v_add_f32_e32 v2, v12, v2
	v_fmac_f32_e32 v8, v87, v87
	v_and_b32_e32 v90, 0xffff0000, v9
	v_add_f32_e32 v2, v8, v2
	v_lshlrev_b32_e32 v89, 16, v9
	v_mul_f32_e32 v8, v90, v90
	v_fmac_f32_e32 v8, v89, v89
	v_and_b32_e32 v92, 0xffff0000, v10
	v_add_f32_e32 v2, v8, v2
	v_lshlrev_b32_e32 v91, 16, v10
	v_mul_f32_e32 v8, v92, v92
	v_fmac_f32_e32 v8, v91, v91
	v_and_b32_e32 v94, 0xffff0000, v11
	v_add_f32_e32 v2, v8, v2
	v_lshlrev_b32_e32 v93, 16, v11
	v_mul_f32_e32 v8, v94, v94
	v_fmac_f32_e32 v8, v93, v93
	s_waitcnt vmcnt(2)
	v_and_b32_e32 v30, 0xffff0000, v4
	v_add_f32_e32 v8, v8, v2
	v_lshlrev_b32_e32 v2, 16, v4
	v_mul_f32_e32 v4, v30, v30
	v_and_b32_e32 v32, 0xffff0000, v5
	v_fmac_f32_e32 v4, v2, v2
	v_lshlrev_b32_e32 v31, 16, v5
	v_mul_f32_e32 v5, v32, v32
	v_add_f32_e32 v4, v4, v8
	v_fmac_f32_e32 v5, v31, v31
	v_and_b32_e32 v34, 0xffff0000, v6
	v_add_f32_e32 v4, v5, v4
	v_lshlrev_b32_e32 v33, 16, v6
	v_mul_f32_e32 v5, v34, v34
	v_fmac_f32_e32 v5, v33, v33
	v_and_b32_e32 v36, 0xffff0000, v7
	v_add_f32_e32 v4, v5, v4
	v_lshlrev_b32_e32 v35, 16, v7
	v_mul_f32_e32 v5, v36, v36
	v_fmac_f32_e32 v5, v35, v35
	v_add_f32_e32 v4, v5, v4
	v_mov_b32_e32 v5, v4
	s_nop 1
	v_permlane32_swap_b32_e32 v4, v5
	v_add_f32_e32 v4, v4, v5
	v_fmamk_f32 v4, v4, 0x3c000000, v216
	v_rsq_f32_e32 v37, v4
	global_load_dwordx4 v[4:7], v[20:21], off offset:256
	global_load_dwordx4 v[12:15], v[20:21], off offset:288
	global_load_dwordx4 v[8:11], v[20:21], off offset:320
	global_load_dwordx4 v[16:19], v[20:21], off offset:352
	v_mul_f32_e32 v37, 0x3dd53b94, v37
	v_mul_f32_e32 v20, v37, v26
	v_mul_f32_e32 v21, v37, v27
	s_waitcnt vmcnt(4)
	v_mul_f32_e32 v20, v38, v20
	v_mul_f32_e32 v21, v39, v21
	v_cvt_pk_bf16_f32 v132, v20, v21
	v_mul_f32_e32 v20, v37, v29
	v_mul_f32_e32 v21, v37, v42
	v_mul_f32_e32 v20, v40, v20
	v_mul_f32_e32 v21, v41, v21
	v_cvt_pk_bf16_f32 v133, v20, v21
	v_mul_f32_e32 v20, v37, v43
	v_mul_f32_e32 v21, v37, v44
	v_mul_f32_e32 v20, v22, v20
	v_mul_f32_e32 v21, v23, v21
	v_cvt_pk_bf16_f32 v134, v20, v21
	v_mul_f32_e32 v20, v37, v45
	v_mul_f32_e32 v21, v37, v46
	v_mul_f32_e32 v20, v24, v20
	v_mul_f32_e32 v21, v25, v21
	v_cvt_pk_bf16_f32 v135, v20, v21
	global_load_dwordx4 v[20:23], v[184:185], off offset:64
	global_load_dwordx4 v[24:27], v[184:185], off offset:80
	v_mul_f32_e32 v29, v37, v47
	v_mul_f32_e32 v38, v37, v56
	v_mul_f32_e32 v39, v37, v57
	v_mul_f32_e32 v40, v37, v58
	v_mul_f32_e32 v41, v37, v59
	v_mul_f32_e32 v42, v37, v60
	v_mul_f32_e32 v43, v37, v61
	v_mul_f32_e32 v44, v37, v62
	v_mul_f32_e32 v2, v37, v2
	s_waitcnt vmcnt(5)
	v_lshlrev_b32_e32 v60, 16, v7
	s_waitcnt vmcnt(4)
	v_lshlrev_b32_e32 v46, 16, v15
	v_and_b32_e32 v56, 0xffff0000, v13
	s_waitcnt vmcnt(2)
	v_lshlrev_b32_e32 v47, 16, v19
	v_and_b32_e32 v57, 0xffff0000, v17
	v_lshlrev_b32_e32 v59, 16, v16
	v_lshlrev_b32_e32 v58, 16, v12
	v_and_b32_e32 v62, 0xffff0000, v7
	v_and_b32_e32 v7, 0xffff0000, v10
	v_lshlrev_b32_e32 v61, 16, v11
	s_waitcnt vmcnt(1)
	v_mul_f32_e32 v20, v20, v29
	v_mul_f32_e32 v29, v37, v48
	v_mul_f32_e32 v21, v21, v29
	v_cvt_pk_bf16_f32 v136, v20, v21
	v_mul_f32_e32 v20, v37, v49
	v_mul_f32_e32 v21, v37, v50
	v_mul_f32_e32 v20, v22, v20
	v_mul_f32_e32 v21, v23, v21
	v_cvt_pk_bf16_f32 v137, v20, v21
	v_mul_f32_e32 v20, v37, v51
	v_mul_f32_e32 v21, v37, v52
	s_waitcnt vmcnt(0)
	v_mul_f32_e32 v20, v20, v24
	v_mul_f32_e32 v21, v21, v25
	v_cvt_pk_bf16_f32 v138, v20, v21
	v_mul_f32_e32 v20, v37, v53
	v_mul_f32_e32 v21, v37, v54
	v_mul_f32_e32 v20, v20, v26
	v_mul_f32_e32 v21, v21, v27
	v_cvt_pk_bf16_f32 v139, v20, v21
	global_load_dwordx4 v[20:23], v[184:185], off offset:128
	global_load_dwordx4 v[24:27], v[184:185], off offset:144
	v_mul_f32_e32 v29, v37, v55
	v_and_b32_e32 v49, 0xffff0000, v19
	v_and_b32_e32 v48, 0xffff0000, v15
	v_lshlrev_b32_e32 v51, 16, v18
	v_lshlrev_b32_e32 v50, 16, v14
	v_and_b32_e32 v53, 0xffff0000, v18
	v_and_b32_e32 v52, 0xffff0000, v14
	v_mul_f32_e32 v14, v37, v30
	v_mul_f32_e32 v15, v37, v31
	v_mul_f32_e32 v18, v37, v32
	v_mul_f32_e32 v19, v37, v33
	v_mul_f32_e32 v30, v37, v34
	v_mul_f32_e32 v31, v37, v35
	v_mul_f32_e32 v32, v37, v36
	v_lshlrev_b32_e32 v55, 16, v17
	v_lshlrev_b32_e32 v54, 16, v13
	v_and_b32_e32 v17, 0xffff0000, v16
	v_and_b32_e32 v16, 0xffff0000, v12
	s_waitcnt vmcnt(1)
	v_mul_f32_e32 v20, v29, v20
	v_mul_f32_e32 v21, v38, v21
	v_mul_f32_e32 v22, v39, v22
	v_mul_f32_e32 v23, v40, v23
	s_waitcnt vmcnt(0)
	v_mul_f32_e32 v24, v41, v24
	v_mul_f32_e32 v25, v42, v25
	v_mul_f32_e32 v26, v43, v26
	v_mul_f32_e32 v27, v44, v27
	v_cvt_pk_bf16_f32 v140, v20, v21
	v_cvt_pk_bf16_f32 v141, v22, v23
	v_cvt_pk_bf16_f32 v142, v24, v25
	v_cvt_pk_bf16_f32 v143, v26, v27
	global_load_dwordx4 v[20:23], v[184:185], off offset:192
	global_load_dwordx4 v[24:27], v[184:185], off offset:208
	v_mul_f32_e32 v29, v37, v63
	v_mul_f32_e32 v38, v37, v64
	v_mul_f32_e32 v39, v37, v65
	v_mul_f32_e32 v40, v37, v66
	v_mul_f32_e32 v41, v37, v67
	v_mul_f32_e32 v42, v37, v68
	v_mul_f32_e32 v43, v37, v69
	v_mul_f32_e32 v44, v37, v70
	v_lshlrev_b32_e32 v65, 16, v10
	v_lshlrev_b32_e32 v10, 16, v5
	v_and_b32_e32 v67, 0xffff0000, v9
	v_and_b32_e32 v66, 0xffff0000, v5
	v_lshlrev_b32_e32 v68, 16, v4
	v_and_b32_e32 v5, 0xffff0000, v8
	v_and_b32_e32 v4, 0xffff0000, v4
	v_and_b32_e32 v63, 0xffff0000, v11
	v_lshlrev_b32_e32 v64, 16, v6
	v_and_b32_e32 v6, 0xffff0000, v6
	v_lshlrev_b32_e32 v11, 16, v9
	v_lshlrev_b32_e32 v69, 16, v8
	v_pk_mul_f32 v[8:9], v[48:49], v[48:49]
	s_waitcnt vmcnt(1)
; __device__ __forceinline__ float bf2f(unsigned b) { return __uint_as_float(b << 16); }
; __device__ __forceinline__ float rsq(float x) { return __builtin_amdgcn_rsqf(x); }
; __device__ __forceinline__ unsigned cvtpk(float lo, float hi) { unsigned r; asm volatile("v_cvt_pk_bf16_f32 %0, %1, %2" : "=v"(r) : "v"(lo), "v"(hi)); return r; }
; template <int layer>
; __device__ __forceinline__ void attn_phase(LAS unsigned char* lds) {
;     ...
;                 for (int d0 = 0; d0 < 8; ++d0) { const f32x4 g0 = *(const f32x4*)(qkg + d0 * 16 + hi * 8), g1 = *(const f32x4*)(qkg + d0 * 16 + hi * 8 + 4); u32x4 o;
; #pragma unroll
;                     for (int j = 0; j < 4; ++j) { const float x0 = bf2f(raw[d0][j] & 0xffffu), x1 = bf2f(raw[d0][j] >> 16); const f32x4 gg = j < 2 ? g0 : g1;
;                         o[j] = cvtpk(x0 * rn * gg[(2 * j) & 3], x1 * rn * gg[(2 * j + 1) & 3]); }
;                     qr[d0] = *reinterpret_cast<bf16x8*>(&o); }
;                 if constexpr (layer == 0) {
;                     float xr[4][8]; float s2 = 0.f;
; #pragma unroll
;                     for (int c = 0; c < 4; ++c)
; #pragma unroll
;                         for (int j = 0; j < 4; ++j) { xr[c][2 * j] = bf2f(raw[8 + c][j] & 0xffffu); xr[c][2 * j + 1] = bf2f(raw[8 + c][j] >> 16); s2 += xr[c][2 * j] * xr[c][2 * j] + xr[c][2 * j + 1] * xr[c][2 * j + 1]; }
;                     { auto rr = __builtin_amdgcn_permlane32_swap(__float_as_uint(s2), __float_as_uint(s2), false, false); s2 = __uint_as_float(rr[0]) + __uint_as_float(rr[1]); }
;                     const float r2 = rsq(s2 * (1.0f / 64) + EPS); const float pos = (float)positions[tq];
; #pragma unroll
;                     for (int c = 0; c < 4; ++c) { const f32x4 g0 = *(const f32x4*)(qkg + 128 + c * 16 + hi * 8), g1 = *(const f32x4*)(qkg + 128 + c * 16 + hi * 8 + 4);
; #pragma unroll
;                         for (int j = 0; j < 8; ++j) xr[c][j] *= r2 * (j < 4 ? g0[j & 3] : g1[j & 3]); }
	v_mul_f32_e32 v20, v29, v20
	v_mul_f32_e32 v21, v38, v21
	v_mul_f32_e32 v22, v39, v22
	v_mul_f32_e32 v23, v40, v23
	s_waitcnt vmcnt(0)
	v_mul_f32_e32 v24, v41, v24
	v_mul_f32_e32 v25, v42, v25
	v_mul_f32_e32 v26, v43, v26
	v_mul_f32_e32 v27, v44, v27
	v_cvt_pk_bf16_f32 v144, v20, v21
	v_cvt_pk_bf16_f32 v145, v22, v23
	v_cvt_pk_bf16_f32 v146, v24, v25
	v_cvt_pk_bf16_f32 v147, v26, v27
	global_load_dwordx4 v[20:23], v[184:185], off offset:256
	global_load_dwordx4 v[24:27], v[184:185], off offset:272
	v_mul_f32_e32 v29, v37, v71
	v_mul_f32_e32 v38, v37, v72
	v_mul_f32_e32 v39, v37, v73
	v_mul_f32_e32 v40, v37, v74
	v_mul_f32_e32 v41, v37, v75
	v_mul_f32_e32 v42, v37, v76
	v_mul_f32_e32 v43, v37, v77
	v_mul_f32_e32 v44, v37, v78
	v_mov_b32_e32 v74, v49
	v_mov_b32_e32 v75, v53
	v_mov_b32_e32 v72, v47
	v_mov_b32_e32 v73, v51
	v_pk_mul_f32 v[74:75], v[74:75], v[74:75]
	v_pk_mul_f32 v[76:77], v[56:57], v[56:57]
	v_pk_fma_f32 v[72:73], v[72:73], v[72:73], v[74:75]
	v_pk_mul_f32 v[70:71], v[52:53], v[52:53]
	v_pk_fma_f32 v[76:77], v[54:55], v[54:55], v[76:77]
	v_pk_fma_f32 v[70:71], v[50:51], v[50:51], v[70:71]
	v_pk_fma_f32 v[8:9], v[46:47], v[46:47], v[8:9]
	s_waitcnt vmcnt(1)
	v_mul_f32_e32 v20, v29, v20
	v_mul_f32_e32 v21, v38, v21
	v_mul_f32_e32 v22, v39, v22
	v_mul_f32_e32 v23, v40, v23
	s_waitcnt vmcnt(0)
	v_mul_f32_e32 v24, v41, v24
	v_mul_f32_e32 v25, v42, v25
	v_mul_f32_e32 v26, v43, v26
	v_mul_f32_e32 v27, v44, v27
	v_cvt_pk_bf16_f32 v148, v20, v21
	v_cvt_pk_bf16_f32 v149, v22, v23
	v_cvt_pk_bf16_f32 v150, v24, v25
	v_cvt_pk_bf16_f32 v151, v26, v27
	global_load_dwordx4 v[20:23], v[184:185], off offset:320
	global_load_dwordx4 v[24:27], v[184:185], off offset:336
	v_mul_f32_e32 v29, v37, v79
	v_mul_f32_e32 v38, v37, v80
	v_mul_f32_e32 v39, v37, v81
	v_mul_f32_e32 v40, v37, v82
	v_mul_f32_e32 v41, v37, v83
	v_mul_f32_e32 v42, v37, v84
	v_mul_f32_e32 v43, v37, v85
	v_mul_f32_e32 v44, v37, v86
	v_mov_b32_e32 v82, v57
	v_mov_b32_e32 v83, v17
	v_mov_b32_e32 v80, v55
	v_mov_b32_e32 v81, v59
	v_pk_mul_f32 v[82:83], v[82:83], v[82:83]
	v_pk_mul_f32 v[84:85], v[62:63], v[62:63]
	v_pk_fma_f32 v[74:75], v[80:81], v[80:81], v[82:83]
	v_pk_mul_f32 v[78:79], v[16:17], v[16:17]
	v_pk_fma_f32 v[84:85], v[60:61], v[60:61], v[84:85]
	v_pk_fma_f32 v[78:79], v[58:59], v[58:59], v[78:79]
	s_waitcnt vmcnt(1)
	v_mul_f32_e32 v20, v29, v20
	v_mul_f32_e32 v21, v38, v21
	v_mul_f32_e32 v22, v39, v22
	v_mul_f32_e32 v23, v40, v23
	s_waitcnt vmcnt(0)
	v_mul_f32_e32 v24, v41, v24
	v_mul_f32_e32 v25, v42, v25
	v_mul_f32_e32 v26, v43, v26
	v_mul_f32_e32 v27, v44, v27
	v_cvt_pk_bf16_f32 v152, v20, v21
	v_cvt_pk_bf16_f32 v153, v22, v23
	v_cvt_pk_bf16_f32 v154, v24, v25
	v_cvt_pk_bf16_f32 v155, v26, v27
	global_load_dwordx4 v[20:23], v[184:185], off offset:384
	global_load_dwordx4 v[24:27], v[184:185], off offset:400
	v_mul_f32_e32 v29, v37, v87
	v_mul_f32_e32 v38, v37, v88
	v_mul_f32_e32 v39, v37, v89
	v_mul_f32_e32 v40, v37, v90
	v_mul_f32_e32 v41, v37, v91
	v_mul_f32_e32 v42, v37, v92
	v_mul_f32_e32 v43, v37, v93
	v_mul_f32_e32 v44, v37, v94
	v_pk_mul_f32 v[88:89], v[66:67], v[66:67]
	v_pk_mul_f32 v[90:91], v[4:5], v[4:5]
	v_pk_mul_f32 v[86:87], v[6:7], v[6:7]
	v_pk_fma_f32 v[88:89], v[10:11], v[10:11], v[88:89]
	v_pk_fma_f32 v[90:91], v[68:69], v[68:69], v[90:91]
	v_pk_fma_f32 v[86:87], v[64:65], v[64:65], v[86:87]
	v_pk_add_f32 v[80:81], v[90:91], v[88:89]
	s_waitcnt vmcnt(1)
	v_mul_f32_e32 v20, v29, v20
	v_mul_f32_e32 v21, v38, v21
	v_mul_f32_e32 v22, v39, v22
	v_mul_f32_e32 v23, v40, v23
	s_waitcnt vmcnt(0)
	v_mul_f32_e32 v24, v41, v24
	v_mul_f32_e32 v25, v42, v25
	v_mul_f32_e32 v26, v43, v26
	v_mul_f32_e32 v27, v44, v27
	v_cvt_pk_bf16_f32 v156, v20, v21
	v_cvt_pk_bf16_f32 v157, v22, v23
	v_cvt_pk_bf16_f32 v158, v24, v25
	v_cvt_pk_bf16_f32 v159, v26, v27
	global_load_dwordx4 v[24:27], v[184:185], off offset:448
	global_load_dwordx4 v[20:23], v[184:185], off offset:464
	v_cndmask_b32_e64 v29, 0, 1, s[18:19]
	v_cmp_ne_u32_e64 s[4:5], 1, v29
	v_mov_b32_e32 v29, s60
	v_lshl_add_u64 v[28:29], v[28:29], 2, s[16:17]
	v_pk_add_f32 v[80:81], v[86:87], v[80:81]
	s_waitcnt vmcnt(1)
	v_mul_f32_e32 v14, v14, v25
	v_mul_f32_e32 v15, v15, v26
	v_mul_f32_e32 v18, v18, v27
	s_waitcnt vmcnt(0)
	v_mul_f32_e32 v19, v19, v20
	v_mul_f32_e32 v20, v30, v21
	v_mul_f32_e32 v21, v31, v22
	v_mul_f32_e32 v22, v32, v23
	v_mul_f32_e32 v2, v2, v24
	v_cvt_pk_bf16_f32 v160, v2, v14
	v_cvt_pk_bf16_f32 v161, v15, v18
	v_cvt_pk_bf16_f32 v162, v19, v20
	v_cvt_pk_bf16_f32 v163, v21, v22
	global_load_dword v92, v[28:29], off
	global_load_dwordx4 v[18:21], v[184:185], off offset:576
	global_load_dwordx4 v[22:25], v[184:185], off offset:592
	s_nop 0
	global_load_dwordx4 v[26:29], v[184:185], off offset:704
	global_load_dwordx4 v[30:33], v[184:185], off offset:720
	global_load_dwordx4 v[12:15], v[184:185], off offset:512
	global_load_dwordx4 v[34:37], v[184:185], off offset:528
	global_load_dwordx4 v[38:41], v[184:185], off offset:640
	global_load_dwordx4 v[42:45], v[184:185], off offset:656
	v_pk_add_f32 v[80:81], v[84:85], v[80:81]
	s_nop 0
	v_pk_add_f32 v[78:79], v[78:79], v[80:81]
	s_nop 0
	v_pk_add_f32 v[76:77], v[76:77], v[78:79]
	s_nop 0
	v_pk_add_f32 v[70:71], v[70:71], v[76:77]
	s_nop 0
	v_pk_add_f32 v[8:9], v[8:9], v[70:71]
	s_waitcnt vmcnt(8)
	v_cvt_f32_i32_e32 v70, v92
	v_pk_add_f32 v[8:9], v[90:91], v[8:9] op_sel:[1,0] op_sel_hi:[0,1]
	v_pk_add_f32 v[8:9], v[88:89], v[8:9] op_sel:[1,0] op_sel_hi:[0,1]
	v_pk_add_f32 v[8:9], v[86:87], v[8:9] op_sel:[1,0] op_sel_hi:[0,1]
	v_pk_add_f32 v[8:9], v[84:85], v[8:9] op_sel:[1,0] op_sel_hi:[0,1]
	v_pk_add_f32 v[8:9], v[74:75], v[8:9] op_sel:[1,0] op_sel_hi:[0,1]
	v_pk_add_f32 v[8:9], v[74:75], v[8:9]
	s_nop 0
	v_pk_add_f32 v[8:9], v[72:73], v[8:9] op_sel:[1,0] op_sel_hi:[0,1]
	v_pk_add_f32 v[8:9], v[72:73], v[8:9]
	s_nop 0
	v_mov_b32_e32 v2, v8
	s_nop 1
	v_permlane32_swap_b32_e32 v8, v2
	v_add_f32_e32 v2, v8, v2
	v_fmamk_f32 v2, v2, 0x3c800000, v216
	v_rsq_f32_e32 v2, v2
	s_waitcnt vmcnt(6)
; __device__ __forceinline__ float rsq(float x) { return __builtin_amdgcn_rsqf(x); }
; template <int layer>
; __device__ __forceinline__ void attn_phase(LAS unsigned char* lds) {
;     ...
;                     const float r2 = rsq(s2 * (1.0f / 64) + EPS); const float pos = (float)positions[tq];
; #pragma unroll
;                     for (int c = 0; c < 4; ++c) { const f32x4 g0 = *(const f32x4*)(qkg + 128 + c * 16 + hi * 8), g1 = *(const f32x4*)(qkg + 128 + c * 16 + hi * 8 + 4);
; #pragma unroll
;                         for (int j = 0; j < 8; ++j) xr[c][j] *= r2 * (j < 4 ? g0[j & 3] : g1[j & 3]); }
; #pragma unroll
;                     for (int c = 0; c < 2; ++c) { u32x4 o1, o2;
; #pragma unroll
;                         for (int jj = 0; jj < 4; ++jj) { float y1[2], y2[2];
; #pragma unroll
;                             for (int e = 0; e < 2; ++e) { const int j = 2 * jj + e; const int i = c * 16 + hi * 8 + j;
;                                 const float freq = exp2f(-(float)i * (13.287712379549449f / 32.0f)); float rev = pos * freq * 0.15915494309189535f; rev -= floorf(rev);
;                                 const float sn = __builtin_amdgcn_sinf(rev), cs = __builtin_amdgcn_cosf(rev);
;                                 y1[e] = (xr[c][j] * cs - xr[c + 2][j] * sn) * C2; y2[e] = (xr[c + 2][j] * cs + xr[c][j] * sn) * C2; }
	v_mov_b32_e32 v8, v24
	s_waitcnt vmcnt(4)
	v_mov_b32_e32 v9, v32
	v_mov_b32_e32 v32, v25
	v_mov_b32_e32 v24, v22
	v_mov_b32_e32 v25, v30
	v_mov_b32_e32 v30, v23
	v_mov_b32_e32 v22, v20
	v_mov_b32_e32 v23, v28
	v_mov_b32_e32 v28, v21
	v_mov_b32_e32 v20, v18
	v_mov_b32_e32 v21, v26
	v_mov_b32_e32 v26, v19
	s_waitcnt vmcnt(2)
	v_mov_b32_e32 v18, v36
	s_waitcnt vmcnt(0)
	v_mov_b32_e32 v19, v44
	v_mov_b32_e32 v44, v37
	v_mov_b32_e32 v36, v34
	v_mov_b32_e32 v37, v42
	v_mov_b32_e32 v42, v35
	v_mov_b32_e32 v34, v14
	v_mov_b32_e32 v35, v40
	v_mov_b32_e32 v40, v15
	v_mov_b32_e32 v14, v12
	v_mov_b32_e32 v15, v38
	v_mov_b32_e32 v38, v13
	v_pk_mul_f32 v[12:13], v[14:15], v[2:3] op_sel_hi:[1,0]
	v_pk_mul_f32 v[14:15], v[38:39], v[2:3] op_sel_hi:[1,0]
	v_pk_mul_f32 v[34:35], v[34:35], v[2:3] op_sel_hi:[1,0]
	v_pk_mul_f32 v[38:39], v[40:41], v[2:3] op_sel_hi:[1,0]
	v_pk_mul_f32 v[36:37], v[36:37], v[2:3] op_sel_hi:[1,0]
	v_pk_mul_f32 v[40:41], v[42:43], v[2:3] op_sel_hi:[1,0]
	v_pk_mul_f32 v[42:43], v[44:45], v[2:3] op_sel_hi:[1,0]
	v_pk_mul_f32 v[26:27], v[26:27], v[2:3] op_sel_hi:[1,0]
	v_pk_mul_f32 v[28:29], v[28:29], v[2:3] op_sel_hi:[1,0]
	v_pk_mul_f32 v[24:25], v[2:3], v[24:25] op_sel_hi:[0,1]
	v_pk_mul_f32 v[30:31], v[2:3], v[30:31] op_sel_hi:[0,1]
	v_pk_mul_f32 v[8:9], v[2:3], v[8:9] op_sel_hi:[0,1]
	v_pk_mul_f32 v[32:33], v[2:3], v[32:33] op_sel_hi:[0,1]
	v_pk_mul_f32 v[18:19], v[18:19], v[2:3] op_sel_hi:[1,0]
	v_pk_mul_f32 v[20:21], v[20:21], v[2:3] op_sel_hi:[1,0]
	v_pk_mul_f32 v[22:23], v[22:23], v[2:3] op_sel_hi:[1,0]
	v_pk_mul_f32 v[4:5], v[14:15], v[4:5]
	v_pk_mul_f32 v[10:11], v[34:35], v[10:11]
	v_pk_mul_f32 v[14:15], v[38:39], v[66:67]
	v_pk_mul_f32 v[34:35], v[36:37], v[64:65]
	v_pk_mul_f32 v[6:7], v[40:41], v[6:7]
	v_pk_mul_f32 v[36:37], v[42:43], v[62:63]
	v_pk_mul_f32 v[16:17], v[26:27], v[16:17]
	v_pk_mul_f32 v[26:27], v[28:29], v[56:57]
	v_pk_mul_f32 v[24:25], v[24:25], v[50:51]
	v_pk_mul_f32 v[28:29], v[30:31], v[52:53]
	v_pk_mul_f32 v[8:9], v[8:9], v[46:47]
	v_pk_mul_f32 v[30:31], v[32:33], v[48:49]
	v_mul_f32_e32 v2, v192, v70
	v_mul_f32_e32 v32, v193, v70
	v_mul_f32_e32 v33, v194, v70
	v_mul_f32_e32 v38, v195, v70
	v_mul_f32_e32 v39, v196, v70
	v_mul_f32_e32 v40, v197, v70
	v_mul_f32_e32 v41, v198, v70
	v_mul_f32_e32 v42, v199, v70
	v_mul_f32_e32 v43, v200, v70
	v_mul_f32_e32 v44, v201, v70
	v_mul_f32_e32 v45, v202, v70
	v_mul_f32_e32 v46, v203, v70
	v_mul_f32_e32 v47, v204, v70
	v_mul_f32_e32 v48, v205, v70
	v_mul_f32_e32 v49, v206, v70
	v_mul_f32_e32 v50, v207, v70
	v_pk_mul_f32 v[18:19], v[18:19], v[60:61]
	v_pk_mul_f32 v[20:21], v[20:21], v[58:59]
	v_pk_mul_f32 v[22:23], v[22:23], v[54:55]
	v_mul_f32_e32 v51, 0.15915494, v2
	v_mul_f32_e32 v52, 0.15915494, v32
	v_mul_f32_e32 v53, 0.15915494, v33
	v_mul_f32_e32 v54, 0.15915494, v38
	v_mul_f32_e32 v55, 0.15915494, v39
	v_mul_f32_e32 v56, 0.15915494, v40
	v_mul_f32_e32 v57, 0.15915494, v41
	v_mul_f32_e32 v58, 0.15915494, v42
	v_mul_f32_e32 v59, 0.15915494, v43
	v_mul_f32_e32 v60, 0.15915494, v44
	v_mul_f32_e32 v61, 0.15915494, v45
	v_mul_f32_e32 v62, 0.15915494, v46
	v_mul_f32_e32 v63, 0.15915494, v47
	v_mul_f32_e32 v64, 0.15915494, v48
	v_mul_f32_e32 v65, 0.15915494, v49
	v_mul_f32_e32 v66, 0.15915494, v50
	v_floor_f32_e32 v51, v51
	v_floor_f32_e32 v52, v52
	v_floor_f32_e32 v53, v53
	v_floor_f32_e32 v54, v54
	v_floor_f32_e32 v55, v55
	v_floor_f32_e32 v56, v56
	v_floor_f32_e32 v57, v57
	v_floor_f32_e32 v58, v58
	v_floor_f32_e32 v59, v59
	v_floor_f32_e32 v60, v60
	v_floor_f32_e32 v61, v61
	v_floor_f32_e32 v62, v62
	v_floor_f32_e32 v63, v63
	v_floor_f32_e32 v64, v64
	v_floor_f32_e32 v65, v65
	v_floor_f32_e32 v66, v66
	v_fma_f32 v2, v2, 0.15915494, -v51
	v_fma_f32 v51, v32, 0.15915494, -v52
	v_fma_f32 v52, v33, 0.15915494, -v53
	v_fma_f32 v53, v38, 0.15915494, -v54
	v_fma_f32 v54, v39, 0.15915494, -v55
	v_fma_f32 v55, v40, 0.15915494, -v56
	v_fma_f32 v56, v41, 0.15915494, -v57
	v_fma_f32 v57, v42, 0.15915494, -v58
	v_fma_f32 v58, v43, 0.15915494, -v59
	v_fma_f32 v59, v44, 0.15915494, -v60
	v_fma_f32 v60, v45, 0.15915494, -v61
	v_fma_f32 v61, v46, 0.15915494, -v62
	v_fma_f32 v62, v47, 0.15915494, -v63
	v_fma_f32 v64, v48, 0.15915494, -v64
	v_fma_f32 v65, v49, 0.15915494, -v65
	v_fma_f32 v66, v50, 0.15915494, -v66
	v_sin_f32_e32 v32, v2
	v_cos_f32_e32 v33, v2
	v_sin_f32_e32 v39, v51
	v_cos_f32_e32 v38, v51
	v_sin_f32_e32 v40, v52
	v_cos_f32_e32 v41, v52
	v_sin_f32_e32 v43, v53
	v_cos_f32_e32 v42, v53
	v_sin_f32_e32 v44, v54
	v_cos_f32_e32 v45, v54
	v_sin_f32_e32 v47, v55
	v_cos_f32_e32 v46, v55
	v_sin_f32_e32 v48, v56
	v_cos_f32_e32 v49, v56
	v_sin_f32_e32 v51, v57
	v_cos_f32_e32 v50, v57
	v_sin_f32_e32 v52, v58
	v_cos_f32_e32 v53, v58
	v_sin_f32_e32 v55, v59
	v_cos_f32_e32 v54, v59
	v_sin_f32_e32 v56, v60
	v_cos_f32_e32 v57, v60
	v_sin_f32_e32 v59, v61
	v_cos_f32_e32 v58, v61
	v_sin_f32_e32 v60, v62
	v_cos_f32_e32 v61, v62
	v_sin_f32_e32 v63, v64
	v_cos_f32_e32 v62, v64
	v_sin_f32_e32 v64, v65
	v_cos_f32_e32 v65, v65
	v_sin_f32_e32 v67, v66
	v_cos_f32_e32 v66, v66
	v_pk_mul_f32 v[12:13], v[12:13], v[68:69]
	v_mov_b32_e32 v68, v33
	v_mov_b32_e32 v69, v32
	v_pk_mul_f32 v[32:33], v[32:33], v[12:13]
	v_pk_mul_f32 v[70:71], v[38:39], v[4:5]
	v_mov_b32_e32 v72, v39
	v_mov_b32_e32 v73, v38
	v_mov_b32_e32 v38, v41
	v_mov_b32_e32 v39, v40
	v_pk_mul_f32 v[74:75], v[42:43], v[14:15]
	v_mov_b32_e32 v76, v43
	v_mov_b32_e32 v77, v42
	v_mov_b32_e32 v42, v45
	v_mov_b32_e32 v43, v44
	v_pk_mul_f32 v[78:79], v[46:47], v[6:7]
	v_mov_b32_e32 v80, v47
	v_mov_b32_e32 v81, v46
	v_mov_b32_e32 v46, v49
	v_mov_b32_e32 v47, v48
	v_pk_mul_f32 v[82:83], v[50:51], v[36:37]
	v_mov_b32_e32 v84, v51
; __device__ __forceinline__ unsigned cvtpk(float lo, float hi) { unsigned r; asm volatile("v_cvt_pk_bf16_f32 %0, %1, %2" : "=v"(r) : "v"(lo), "v"(hi)); return r; }
; template <int layer>
; __device__ __forceinline__ void attn_phase(LAS unsigned char* lds) {
;     ...
;                             for (int e = 0; e < 2; ++e) { const int j = 2 * jj + e; const int i = c * 16 + hi * 8 + j;
;                                 const float freq = exp2f(-(float)i * (13.287712379549449f / 32.0f)); float rev = pos * freq * 0.15915494309189535f; rev -= floorf(rev);
;                                 const float sn = __builtin_amdgcn_sinf(rev), cs = __builtin_amdgcn_cosf(rev);
;                                 y1[e] = (xr[c][j] * cs - xr[c + 2][j] * sn) * C2; y2[e] = (xr[c + 2][j] * cs + xr[c][j] * sn) * C2; }
;                             o1[jj] = cvtpk(y1[0], y1[1]); o2[jj] = cvtpk(y2[0], y2[1]); }
;                         qr[8 + c] = *reinterpret_cast<bf16x8*>(&o1); qr[10 + c] = *reinterpret_cast<bf16x8*>(&o2); }
;                 }
;             }
;             float m_reg = 0.f, l_reg = 0.f; f32x16 o[4];
; #pragma unroll
;             for (int d0 = 0; d0 < 4; ++d0)
; #pragma unroll
;                 for (int r = 0; r < 16; ++r) o[d0][r] = 0.f;
;     ...
;             FA_ISSUE(0, 0);
;             for (int t = 0; t < NT; t += 2) { FA_STEP(t, 0); FA_STEP(t + 1, 1); }
	v_mov_b32_e32 v85, v50
	v_mov_b32_e32 v50, v53
	v_mov_b32_e32 v51, v52
	v_pk_mul_f32 v[86:87], v[54:55], v[16:17]
	v_mov_b32_e32 v88, v55
	v_mov_b32_e32 v89, v54
	v_mov_b32_e32 v54, v57
	v_mov_b32_e32 v55, v56
	v_pk_mul_f32 v[90:91], v[58:59], v[26:27]
	v_mov_b32_e32 v92, v59
	v_mov_b32_e32 v93, v58
	v_mov_b32_e32 v58, v61
	v_mov_b32_e32 v59, v60
	v_pk_mul_f32 v[94:95], v[62:63], v[28:29]
	v_mov_b32_e32 v96, v63
	v_mov_b32_e32 v97, v62
	v_mov_b32_e32 v62, v65
	v_mov_b32_e32 v63, v64
	v_mov_b32_e32 v100, v67
	v_mov_b32_e32 v101, v66
	v_pk_mul_f32 v[40:41], v[40:41], v[10:11]
	v_pk_mul_f32 v[44:45], v[44:45], v[34:35]
	v_pk_mul_f32 v[48:49], v[48:49], v[18:19]
	v_pk_mul_f32 v[52:53], v[52:53], v[20:21]
	v_pk_mul_f32 v[56:57], v[56:57], v[22:23]
	v_pk_mul_f32 v[60:61], v[60:61], v[24:25]
	v_pk_mul_f32 v[64:65], v[64:65], v[8:9]
	v_pk_mul_f32 v[98:99], v[66:67], v[30:31]
	v_pk_mul_f32 v[12:13], v[68:69], v[12:13]
	v_add_f32_e32 v2, v32, v33
	v_pk_mul_f32 v[4:5], v[72:73], v[4:5]
	v_pk_mul_f32 v[10:11], v[38:39], v[10:11]
	v_pk_mul_f32 v[14:15], v[76:77], v[14:15]
	v_pk_mul_f32 v[32:33], v[42:43], v[34:35]
	v_pk_mul_f32 v[6:7], v[80:81], v[6:7]
	v_pk_mul_f32 v[18:19], v[46:47], v[18:19]
	v_pk_mul_f32 v[34:35], v[84:85], v[36:37]
	v_pk_mul_f32 v[20:21], v[50:51], v[20:21]
	v_pk_mul_f32 v[16:17], v[88:89], v[16:17]
	v_pk_mul_f32 v[22:23], v[54:55], v[22:23]
	v_pk_mul_f32 v[26:27], v[92:93], v[26:27]
	v_pk_mul_f32 v[24:25], v[58:59], v[24:25]
	v_pk_mul_f32 v[28:29], v[96:97], v[28:29]
	v_pk_mul_f32 v[8:9], v[62:63], v[8:9]
	v_pk_mul_f32 v[30:31], v[100:101], v[30:31]
	v_sub_f32_e32 v66, v70, v71
	v_add_f32_e32 v38, v40, v41
	v_sub_f32_e32 v39, v74, v75
	v_add_f32_e32 v40, v44, v45
	v_sub_f32_e32 v41, v78, v79
	v_add_f32_e32 v42, v48, v49
	v_sub_f32_e32 v43, v82, v83
	v_add_f32_e32 v36, v52, v53
	v_sub_f32_e32 v37, v86, v87
	v_add_f32_e32 v44, v56, v57
	v_sub_f32_e32 v45, v90, v91
	v_add_f32_e32 v46, v60, v61
	v_sub_f32_e32 v47, v94, v95
	v_add_f32_e32 v48, v64, v65
	v_sub_f32_e32 v49, v98, v99
	v_sub_f32_e32 v12, v12, v13
	v_add_f32_e32 v4, v4, v5
	v_sub_f32_e32 v5, v10, v11
	v_add_f32_e32 v14, v14, v15
	v_sub_f32_e32 v15, v32, v33
	v_add_f32_e32 v6, v6, v7
	v_sub_f32_e32 v7, v18, v19
	v_add_f32_e32 v34, v34, v35
	v_sub_f32_e32 v20, v20, v21
	v_add_f32_e32 v16, v16, v17
	v_sub_f32_e32 v17, v22, v23
	v_add_f32_e32 v26, v26, v27
	v_sub_f32_e32 v24, v24, v25
	v_add_f32_e32 v28, v28, v29
	v_sub_f32_e32 v8, v8, v9
	v_add_f32_e32 v30, v30, v31
	v_mul_f32_e32 v2, 0x3dd53b94, v2
	v_mul_f32_e32 v13, 0x3dd53b94, v66
	v_mul_f32_e32 v10, 0x3dd53b94, v38
	v_mul_f32_e32 v11, 0x3dd53b94, v39
	v_mul_f32_e32 v32, 0x3dd53b94, v40
	v_mul_f32_e32 v33, 0x3dd53b94, v41
	v_mul_f32_e32 v18, 0x3dd53b94, v42
	v_mul_f32_e32 v19, 0x3dd53b94, v43
	v_mul_f32_e32 v21, 0x3dd53b94, v36
	v_mul_f32_e32 v35, 0x3dd53b94, v37
	v_mul_f32_e32 v22, 0x3dd53b94, v44
	v_mul_f32_e32 v23, 0x3dd53b94, v45
	v_mul_f32_e32 v25, 0x3dd53b94, v46
	v_mul_f32_e32 v27, 0x3dd53b94, v47
	v_mul_f32_e32 v9, 0x3dd53b94, v48
	v_mul_f32_e32 v29, 0x3dd53b94, v49
	v_mul_f32_e32 v12, 0x3dd53b94, v12
	v_mul_f32_e32 v4, 0x3dd53b94, v4
	v_mul_f32_e32 v5, 0x3dd53b94, v5
	v_mul_f32_e32 v14, 0x3dd53b94, v14
	v_mul_f32_e32 v15, 0x3dd53b94, v15
	v_mul_f32_e32 v6, 0x3dd53b94, v6
	v_mul_f32_e32 v7, 0x3dd53b94, v7
	v_mul_f32_e32 v31, 0x3dd53b94, v34
	v_mul_f32_e32 v20, 0x3dd53b94, v20
	v_mul_f32_e32 v16, 0x3dd53b94, v16
	v_mul_f32_e32 v17, 0x3dd53b94, v17
	v_mul_f32_e32 v26, 0x3dd53b94, v26
	v_mul_f32_e32 v24, 0x3dd53b94, v24
	v_mul_f32_e32 v28, 0x3dd53b94, v28
	v_mul_f32_e32 v8, 0x3dd53b94, v8
	v_mul_f32_e32 v30, 0x3dd53b94, v30
	v_cvt_pk_bf16_f32 v164, v12, v13
	v_cvt_pk_bf16_f32 v168, v2, v4
	v_cvt_pk_bf16_f32 v165, v5, v11
	v_cvt_pk_bf16_f32 v169, v10, v14
	v_cvt_pk_bf16_f32 v166, v15, v33
	v_cvt_pk_bf16_f32 v170, v32, v6
	v_cvt_pk_bf16_f32 v167, v7, v19
	v_cvt_pk_bf16_f32 v171, v18, v31
	v_cvt_pk_bf16_f32 v172, v20, v35
	v_cvt_pk_bf16_f32 v176, v21, v16
	v_cvt_pk_bf16_f32 v173, v17, v23
	v_cvt_pk_bf16_f32 v177, v22, v26
	v_cvt_pk_bf16_f32 v174, v24, v27
	v_cvt_pk_bf16_f32 v178, v25, v28
	v_cvt_pk_bf16_f32 v175, v8, v29
	v_cvt_pk_bf16_f32 v179, v9, v30
.LBB0_531:
	v_mov_b32_e32 v16, v3
	v_mov_b32_e32 v17, v3
	v_mov_b32_e32 v2, v3
	v_mov_b32_e32 v4, v3
	v_mov_b32_e32 v5, v3
	v_mov_b32_e32 v6, v3
	v_mov_b32_e32 v7, v3
	v_mov_b32_e32 v8, v3
	v_mov_b32_e32 v9, v3
	v_mov_b32_e32 v10, v3
	v_mov_b32_e32 v11, v3
	v_mov_b32_e32 v12, v3
	v_mov_b32_e32 v13, v3
	v_mov_b32_e32 v14, v3
	v_mov_b32_e32 v15, v3
	v_mov_b64_e32 v[66:67], v[16:17]
	v_mov_b64_e32 v[50:51], v[16:17]
	v_mov_b64_e32 v[34:35], v[16:17]
	s_lshr_b32 s29, s8, 6
	v_readlane_b32 s52, v252, 35
	v_readlane_b32 s54, v252, 33
	v_mov_b64_e32 v[64:65], v[14:15]
	v_mov_b64_e32 v[62:63], v[12:13]
	v_mov_b64_e32 v[60:61], v[10:11]
	v_mov_b64_e32 v[58:59], v[8:9]
	v_mov_b64_e32 v[56:57], v[6:7]
	v_mov_b64_e32 v[54:55], v[4:5]
	v_mov_b64_e32 v[52:53], v[2:3]
	v_mov_b64_e32 v[48:49], v[14:15]
	v_mov_b64_e32 v[46:47], v[12:13]
	v_mov_b64_e32 v[44:45], v[10:11]
	v_mov_b64_e32 v[42:43], v[8:9]
	v_mov_b64_e32 v[40:41], v[6:7]
	v_mov_b64_e32 v[38:39], v[4:5]
	v_mov_b64_e32 v[36:37], v[2:3]
	v_mov_b64_e32 v[32:33], v[14:15]
	v_mov_b64_e32 v[30:31], v[12:13]
	v_mov_b64_e32 v[28:29], v[10:11]
	v_mov_b64_e32 v[26:27], v[8:9]
	v_mov_b64_e32 v[24:25], v[6:7]
	v_mov_b64_e32 v[22:23], v[4:5]
	v_mov_b64_e32 v[20:21], v[2:3]
	v_mov_b64_e32 v[18:19], v[16:17]
	s_xor_b64 s[48:49], s[6:7], -1
	s_add_i32 s29, s29, 4
	s_or_b32 s16, s28, 31
	v_add_u32_e32 v220, s8, v215
	s_mov_b32 s17, 0
	v_mov_b32_e32 v223, 0
	s_mov_b32 s63, 63
	s_mov_b64 s[50:51], s[46:47]
	v_readlane_b32 s53, v252, 36
	v_readlane_b32 s55, v252, 34
	v_mov_b64_e32 v[16:17], v[14:15]
	v_mov_b64_e32 v[14:15], v[12:13]
	v_mov_b64_e32 v[12:13], v[10:11]
	v_mov_b64_e32 v[10:11], v[8:9]
	v_mov_b64_e32 v[8:9], v[6:7]
	v_mov_b64_e32 v[6:7], v[4:5]
	v_mov_b64_e32 v[4:5], v[2:3]
	v_mov_b32_e32 v221, 0
	s_mov_b32 s58, 0
	s_branch .LBB0_534

; __device__ __forceinline__ float bf2f(unsigned b) { return __uint_as_float(b << 16); }
; template <int layer>
; __device__ __forceinline__ void attn_phase(LAS unsigned char* lds) {
;     ...
;                 const size_t tq = (size_t)b * SEQ + qlo + r32;
;                 const bf16* qp = Qs + tq * QLD + h * QHS + hi * 8;
;                 u32x4 raw[NQ];
; #pragma unroll
;                 for (int d0 = 0; d0 < NQ; ++d0) raw[d0] = *(const u32x4*)(qp + d0 * 16);
;                 float ss = 0.f;
; #pragma unroll
;                 for (int d0 = 0; d0 < 8; ++d0)
; #pragma unroll
;                     for (int j = 0; j < 4; ++j) { const float x0 = bf2f(raw[d0][j] & 0xffffu), x1 = bf2f(raw[d0][j] >> 16); ss += x0 * x0 + x1 * x1; }
;                 { auto rr = __builtin_amdgcn_permlane32_swap(__float_as_uint(ss), __float_as_uint(ss), false, false); ss = __uint_as_float(rr[0]) + __uint_as_float(rr[1]); }
.LBB0_1422:
	s_andn2_b64 vcc, exec, s[20:21]
	s_cbranch_vccnz .Lskip_issue0_a1
	s_mov_b32 m0, s77
	s_nop 0
	global_load_lds_dwordx4 v1, s[36:37]
	s_mov_b32 m0, s84
	s_nop 0
	global_load_lds_dwordx4 v178, s[36:37]
	s_mov_b32 m0, s85
	s_nop 0
	global_load_lds_dwordx4 v179, s[36:37]
	s_mov_b32 m0, s86
	s_nop 0
	global_load_lds_dwordx4 v180, s[36:37]
	s_mov_b32 m0, s78
	s_nop 0
	global_load_lds_dwordx4 v133, s[38:39]
	s_mov_b32 m0, s76
	s_nop 0
	global_load_lds_dwordx4 v181, s[38:39]
	s_mov_b32 m0, s87
	s_nop 0
	global_load_lds_dwordx4 v182, s[38:39]
	s_mov_b32 m0, s88
	s_nop 0
	global_load_lds_dwordx4 v183, s[38:39]
.Lskip_issue0_a1:
	s_and_b64 s[4:5], s[8:9], exec
	v_readlane_b32 s4, v252, 28
	v_readlane_b32 s5, v252, 31
	s_cselect_b32 s10, s5, s4
	v_readlane_b32 s4, v252, 23
	s_add_i32 s40, s10, s4
	s_ashr_i32 s4, s40, 31
	s_add_u32 s68, s34, s40
	s_addc_u32 s69, s35, s4
	v_mov_b32_e32 v5, s69
	v_or_b32_e32 v4, s68, v132
	v_lshlrev_b64 v[4:5], 14, v[4:5]
	v_lshl_add_u64 v[4:5], v[138:139], 0, v[4:5]
	global_load_dwordx4 v[20:23], v[4:5], off
	global_load_dwordx4 v[24:27], v[4:5], off offset:32
	global_load_dwordx4 v[28:31], v[4:5], off offset:64
	global_load_dwordx4 v[32:35], v[4:5], off offset:96
	global_load_dwordx4 v[16:19], v[4:5], off offset:128
	global_load_dwordx4 v[12:15], v[4:5], off offset:160
	global_load_dwordx4 v[8:11], v[4:5], off offset:192
	s_nop 0
	global_load_dwordx4 v[4:7], v[4:5], off offset:224
	v_cmp_ne_u32_e64 s[4:5], 1, v186
	s_andn2_b64 vcc, exec, s[20:21]
	v_cmp_ne_u32_e64 s[6:7], 1, v187
	s_waitcnt vmcnt(7)
	v_and_b32_e32 v36, 0xffff0000, v20
	v_and_b32_e32 v38, 0xffff0000, v21
	v_lshlrev_b32_e32 v2, 16, v20
	v_lshlrev_b32_e32 v37, 16, v21
	v_and_b32_e32 v40, 0xffff0000, v22
	v_mul_f32_e32 v20, v36, v36
	v_mul_f32_e32 v21, v38, v38
	v_lshlrev_b32_e32 v39, 16, v22
	v_and_b32_e32 v42, 0xffff0000, v23
	v_mul_f32_e32 v22, v40, v40
	v_fmac_f32_e32 v20, v2, v2
	v_fmac_f32_e32 v21, v37, v37
	v_lshlrev_b32_e32 v41, 16, v23
	s_waitcnt vmcnt(6)
	v_and_b32_e32 v44, 0xffff0000, v24
	v_mul_f32_e32 v23, v42, v42
	v_fmac_f32_e32 v22, v39, v39
	v_add_f32_e32 v20, v20, v21
	v_lshlrev_b32_e32 v43, 16, v24
	v_and_b32_e32 v46, 0xffff0000, v25
	v_mul_f32_e32 v24, v44, v44
	v_fmac_f32_e32 v23, v41, v41
	v_add_f32_e32 v20, v22, v20
	v_lshlrev_b32_e32 v45, 16, v25
	v_and_b32_e32 v48, 0xffff0000, v26
	v_mul_f32_e32 v25, v46, v46
	v_fmac_f32_e32 v24, v43, v43
	v_add_f32_e32 v20, v23, v20
	v_lshlrev_b32_e32 v47, 16, v26
	v_and_b32_e32 v50, 0xffff0000, v27
	v_mul_f32_e32 v26, v48, v48
	v_fmac_f32_e32 v25, v45, v45
	v_add_f32_e32 v20, v24, v20
	v_lshlrev_b32_e32 v49, 16, v27
	s_waitcnt vmcnt(5)
	v_lshlrev_b32_e32 v51, 16, v28
	v_and_b32_e32 v28, 0xffff0000, v28
	v_mul_f32_e32 v27, v50, v50
	v_fmac_f32_e32 v26, v47, v47
	v_add_f32_e32 v20, v25, v20
	v_lshlrev_b32_e32 v52, 16, v29
	v_and_b32_e32 v29, 0xffff0000, v29
	v_mul_f32_e32 v62, v28, v28
	v_fmac_f32_e32 v27, v49, v49
	v_add_f32_e32 v20, v26, v20
	v_lshlrev_b32_e32 v53, 16, v30
	v_and_b32_e32 v30, 0xffff0000, v30
	v_mul_f32_e32 v63, v29, v29
	v_fmac_f32_e32 v62, v51, v51
	v_add_f32_e32 v20, v27, v20
	v_lshlrev_b32_e32 v54, 16, v31
	v_and_b32_e32 v31, 0xffff0000, v31
	v_mul_f32_e32 v64, v30, v30
	v_fmac_f32_e32 v63, v52, v52
	v_add_f32_e32 v20, v62, v20
	s_waitcnt vmcnt(4)
	v_lshlrev_b32_e32 v55, 16, v32
	v_and_b32_e32 v32, 0xffff0000, v32
	v_mul_f32_e32 v65, v31, v31
	v_fmac_f32_e32 v64, v53, v53
	v_add_f32_e32 v20, v63, v20
	v_lshlrev_b32_e32 v56, 16, v33
	v_and_b32_e32 v33, 0xffff0000, v33
	v_mul_f32_e32 v66, v32, v32
	v_fmac_f32_e32 v65, v54, v54
	v_add_f32_e32 v20, v64, v20
	v_lshlrev_b32_e32 v57, 16, v34
	v_and_b32_e32 v34, 0xffff0000, v34
	v_mul_f32_e32 v67, v33, v33
	v_fmac_f32_e32 v66, v55, v55
	v_add_f32_e32 v20, v65, v20
	v_lshlrev_b32_e32 v58, 16, v35
	v_and_b32_e32 v35, 0xffff0000, v35
	v_mul_f32_e32 v68, v34, v34
	v_fmac_f32_e32 v67, v56, v56
	v_add_f32_e32 v20, v66, v20
	s_waitcnt vmcnt(3)
	v_lshlrev_b32_e32 v59, 16, v16
	v_and_b32_e32 v16, 0xffff0000, v16
	v_mul_f32_e32 v69, v35, v35
	v_fmac_f32_e32 v68, v57, v57
	v_add_f32_e32 v20, v67, v20
	v_lshlrev_b32_e32 v60, 16, v17
	v_and_b32_e32 v17, 0xffff0000, v17
	v_mul_f32_e32 v70, v16, v16
	v_fmac_f32_e32 v69, v58, v58
	v_add_f32_e32 v20, v68, v20
	v_mul_f32_e32 v71, v17, v17
	v_fmac_f32_e32 v70, v59, v59
	v_add_f32_e32 v20, v69, v20
	v_fmac_f32_e32 v71, v60, v60
	v_add_f32_e32 v20, v70, v20
	v_add_f32_e32 v62, v71, v20
	global_load_dwordx4 v[20:23], v[136:137], off offset:16
	global_load_dwordx4 v[24:27], v[136:137], off
	v_lshlrev_b32_e32 v61, 16, v18
	v_and_b32_e32 v18, 0xffff0000, v18
	v_mul_f32_e32 v63, v18, v18
	v_fmac_f32_e32 v63, v61, v61
	v_add_f32_e32 v62, v63, v62
	v_lshlrev_b32_e32 v63, 16, v19
	v_and_b32_e32 v19, 0xffff0000, v19
	v_mul_f32_e32 v64, v19, v19
	v_fmac_f32_e32 v64, v63, v63
	v_add_f32_e32 v62, v64, v62
	s_waitcnt vmcnt(4)
	v_lshlrev_b32_e32 v64, 16, v12
	v_and_b32_e32 v12, 0xffff0000, v12
	v_mul_f32_e32 v65, v12, v12
	v_fmac_f32_e32 v65, v64, v64
	v_add_f32_e32 v62, v65, v62
	v_lshlrev_b32_e32 v65, 16, v13
	v_and_b32_e32 v13, 0xffff0000, v13
	v_mul_f32_e32 v66, v13, v13
	v_fmac_f32_e32 v66, v65, v65
	v_add_f32_e32 v62, v66, v62
	v_lshlrev_b32_e32 v66, 16, v14
	v_and_b32_e32 v14, 0xffff0000, v14
	v_mul_f32_e32 v67, v14, v14
	v_fmac_f32_e32 v67, v66, v66
	v_add_f32_e32 v62, v67, v62
	v_lshlrev_b32_e32 v67, 16, v15
	v_and_b32_e32 v15, 0xffff0000, v15
	v_mul_f32_e32 v68, v15, v15
	v_fmac_f32_e32 v68, v67, v67
	s_waitcnt vmcnt(3)
; __device__ __forceinline__ float bf2f(unsigned b) { return __uint_as_float(b << 16); }
; __device__ __forceinline__ float rsq(float x) { return __builtin_amdgcn_rsqf(x); }
; __device__ __forceinline__ unsigned cvtpk(float lo, float hi) { unsigned r; asm volatile("v_cvt_pk_bf16_f32 %0, %1, %2" : "=v"(r) : "v"(lo), "v"(hi)); return r; }
; template <int layer>
; __device__ __forceinline__ void attn_phase(LAS unsigned char* lds) {
;     ...
;                 { auto rr = __builtin_amdgcn_permlane32_swap(__float_as_uint(ss), __float_as_uint(ss), false, false); ss = __uint_as_float(rr[0]) + __uint_as_float(rr[1]); }
;                 const float rn = rsq(ss * (1.0f / 128) + EPS) * C2;
; #pragma unroll
;                 for (int d0 = 0; d0 < 8; ++d0) { const f32x4 g0 = *(const f32x4*)(qkg + d0 * 16 + hi * 8), g1 = *(const f32x4*)(qkg + d0 * 16 + hi * 8 + 4); u32x4 o;
; #pragma unroll
;                     for (int j = 0; j < 4; ++j) { const float x0 = bf2f(raw[d0][j] & 0xffffu), x1 = bf2f(raw[d0][j] >> 16); const f32x4 gg = j < 2 ? g0 : g1;
;                         o[j] = cvtpk(x0 * rn * gg[(2 * j) & 3], x1 * rn * gg[(2 * j + 1) & 3]); }
;                     qr[d0] = *reinterpret_cast<bf16x8*>(&o); }
	v_and_b32_e32 v69, 0xffff0000, v8
	v_add_f32_e32 v62, v68, v62
	v_lshlrev_b32_e32 v68, 16, v8
	v_mul_f32_e32 v8, v69, v69
	v_fmac_f32_e32 v8, v68, v68
	v_and_b32_e32 v70, 0xffff0000, v9
	v_add_f32_e32 v8, v8, v62
	v_lshlrev_b32_e32 v62, 16, v9
	v_mul_f32_e32 v9, v70, v70
	v_fmac_f32_e32 v9, v62, v62
	v_and_b32_e32 v72, 0xffff0000, v10
	v_add_f32_e32 v8, v9, v8
	v_lshlrev_b32_e32 v71, 16, v10
	v_mul_f32_e32 v9, v72, v72
	v_fmac_f32_e32 v9, v71, v71
	v_and_b32_e32 v74, 0xffff0000, v11
	v_add_f32_e32 v8, v9, v8
	v_lshlrev_b32_e32 v73, 16, v11
	v_mul_f32_e32 v9, v74, v74
	s_waitcnt vmcnt(2)
	v_and_b32_e32 v76, 0xffff0000, v4
	v_fmac_f32_e32 v9, v73, v73
	v_lshlrev_b32_e32 v75, 16, v4
	v_mul_f32_e32 v4, v76, v76
	v_and_b32_e32 v78, 0xffff0000, v5
	v_add_f32_e32 v8, v9, v8
	v_fmac_f32_e32 v4, v75, v75
	v_lshlrev_b32_e32 v77, 16, v5
	v_mul_f32_e32 v5, v78, v78
	v_add_f32_e32 v4, v4, v8
	v_fmac_f32_e32 v5, v77, v77
	v_and_b32_e32 v80, 0xffff0000, v6
	v_add_f32_e32 v4, v5, v4
	v_lshlrev_b32_e32 v79, 16, v6
	v_mul_f32_e32 v5, v80, v80
	v_fmac_f32_e32 v5, v79, v79
	v_and_b32_e32 v82, 0xffff0000, v7
	v_add_f32_e32 v4, v5, v4
	v_lshlrev_b32_e32 v81, 16, v7
	v_mul_f32_e32 v5, v82, v82
	v_fmac_f32_e32 v5, v81, v81
	v_add_f32_e32 v4, v5, v4
	v_mov_b32_e32 v5, v4
	s_nop 1
	v_permlane32_swap_b32_e32 v4, v5
	v_add_f32_e32 v4, v4, v5
	v_fmamk_f32 v4, v4, 0x3c000000, v185
	v_rsq_f32_e32 v4, v4
	s_nop 0
	v_mul_f32_e32 v83, 0x3e0293ee, v4
	v_mul_f32_e32 v4, v83, v36
	v_mul_f32_e32 v2, v83, v2
	s_waitcnt vmcnt(0)
	v_mul_f32_e32 v4, v25, v4
	v_mul_f32_e32 v2, v24, v2
	v_cvt_pk_bf16_f32 v100, v2, v4
	v_mul_f32_e32 v4, v83, v38
	v_mul_f32_e32 v2, v83, v37
	v_mul_f32_e32 v4, v27, v4
	v_mul_f32_e32 v2, v26, v2
	v_cvt_pk_bf16_f32 v101, v2, v4
	v_mul_f32_e32 v4, v83, v40
	v_mul_f32_e32 v2, v83, v39
	v_mul_f32_e32 v4, v21, v4
	v_mul_f32_e32 v2, v20, v2
	v_cvt_pk_bf16_f32 v102, v2, v4
	v_mul_f32_e32 v4, v83, v42
	v_mul_f32_e32 v2, v83, v41
	v_mul_f32_e32 v4, v23, v4
	v_mul_f32_e32 v2, v22, v2
	v_cvt_pk_bf16_f32 v103, v2, v4
	global_load_dwordx4 v[4:7], v[136:137], off offset:64
	global_load_dwordx4 v[8:11], v[136:137], off offset:80
	v_mul_f32_e32 v2, v83, v43
	v_mul_f32_e32 v20, v83, v44
	v_mul_f32_e32 v22, v83, v46
	v_mul_f32_e32 v21, v83, v45
	v_mul_f32_e32 v23, v83, v53
	v_mul_f32_e32 v24, v83, v30
	v_mul_f32_e32 v25, v83, v54
	v_mul_f32_e32 v26, v83, v31
	v_mul_f32_e32 v16, v83, v16
	v_mul_f32_e32 v17, v83, v17
	v_mul_f32_e32 v18, v83, v18
	v_mul_f32_e32 v19, v83, v19
	v_mul_f32_e32 v12, v83, v12
	v_mul_f32_e32 v13, v83, v13
	v_mul_f32_e32 v14, v83, v14
	v_mul_f32_e32 v15, v83, v15
	s_waitcnt vmcnt(1)
	v_mul_f32_e32 v2, v4, v2
	v_mul_f32_e32 v4, v5, v20
	v_cvt_pk_bf16_f32 v104, v2, v4
	v_mul_f32_e32 v2, v7, v22
	v_mul_f32_e32 v4, v83, v48
	v_mul_f32_e32 v5, v6, v21
	v_cvt_pk_bf16_f32 v105, v5, v2
	v_mul_f32_e32 v2, v83, v47
	s_waitcnt vmcnt(0)
	v_mul_f32_e32 v4, v4, v9
	v_mul_f32_e32 v2, v2, v8
	v_cvt_pk_bf16_f32 v106, v2, v4
	v_mul_f32_e32 v4, v83, v50
	v_mul_f32_e32 v2, v83, v49
	v_mul_f32_e32 v4, v4, v11
	v_mul_f32_e32 v2, v2, v10
	v_cvt_pk_bf16_f32 v107, v2, v4
	global_load_dwordx4 v[4:7], v[136:137], off offset:128
	global_load_dwordx4 v[8:11], v[136:137], off offset:144
	v_mul_f32_e32 v2, v83, v51
	v_mul_f32_e32 v20, v83, v28
	v_mul_f32_e32 v21, v83, v52
	v_mul_f32_e32 v22, v83, v29
	s_waitcnt vmcnt(1)
	v_mul_f32_e32 v2, v2, v4
	v_mul_f32_e32 v4, v20, v5
	v_mul_f32_e32 v5, v21, v6
	v_mul_f32_e32 v6, v22, v7
	s_waitcnt vmcnt(0)
; __device__ __forceinline__ float bf2f(unsigned b) { return __uint_as_float(b << 16); }
; __device__ __forceinline__ unsigned cvtpk(float lo, float hi) { unsigned r; asm volatile("v_cvt_pk_bf16_f32 %0, %1, %2" : "=v"(r) : "v"(lo), "v"(hi)); return r; }
; template <int layer>
; __device__ __forceinline__ void attn_phase(LAS unsigned char* lds) {
;     ...
;                 for (int d0 = 0; d0 < 8; ++d0) { const f32x4 g0 = *(const f32x4*)(qkg + d0 * 16 + hi * 8), g1 = *(const f32x4*)(qkg + d0 * 16 + hi * 8 + 4); u32x4 o;
; #pragma unroll
;                     for (int j = 0; j < 4; ++j) { const float x0 = bf2f(raw[d0][j] & 0xffffu), x1 = bf2f(raw[d0][j] >> 16); const f32x4 gg = j < 2 ? g0 : g1;
;                         o[j] = cvtpk(x0 * rn * gg[(2 * j) & 3], x1 * rn * gg[(2 * j + 1) & 3]); }
;                     qr[d0] = *reinterpret_cast<bf16x8*>(&o); }
	v_mul_f32_e32 v7, v23, v8
	v_mul_f32_e32 v8, v24, v9
	v_mul_f32_e32 v9, v25, v10
	v_mul_f32_e32 v10, v26, v11
	v_cvt_pk_bf16_f32 v108, v2, v4
	v_cvt_pk_bf16_f32 v109, v5, v6
	v_cvt_pk_bf16_f32 v110, v7, v8
	v_cvt_pk_bf16_f32 v111, v9, v10
	global_load_dwordx4 v[4:7], v[136:137], off offset:192
	global_load_dwordx4 v[8:11], v[136:137], off offset:208
	v_mul_f32_e32 v2, v83, v55
	v_mul_f32_e32 v20, v83, v32
	v_mul_f32_e32 v21, v83, v56
	v_mul_f32_e32 v22, v83, v33
	v_mul_f32_e32 v23, v83, v57
	v_mul_f32_e32 v24, v83, v34
	v_mul_f32_e32 v25, v83, v58
	v_mul_f32_e32 v26, v83, v35
	s_waitcnt vmcnt(1)
	v_mul_f32_e32 v2, v2, v4
	v_mul_f32_e32 v4, v20, v5
	v_mul_f32_e32 v5, v21, v6
	v_mul_f32_e32 v6, v22, v7
	s_waitcnt vmcnt(0)
	v_mul_f32_e32 v7, v23, v8
	v_mul_f32_e32 v8, v24, v9
	v_mul_f32_e32 v9, v25, v10
	v_mul_f32_e32 v10, v26, v11
	v_cvt_pk_bf16_f32 v112, v2, v4
	v_cvt_pk_bf16_f32 v113, v5, v6
	v_cvt_pk_bf16_f32 v114, v7, v8
	v_cvt_pk_bf16_f32 v115, v9, v10
	global_load_dwordx4 v[4:7], v[136:137], off offset:256
	global_load_dwordx4 v[8:11], v[136:137], off offset:272
	v_mul_f32_e32 v2, v83, v59
	v_mul_f32_e32 v20, v83, v60
	v_mul_f32_e32 v21, v83, v61
	v_mul_f32_e32 v22, v83, v63
	s_waitcnt vmcnt(1)
	v_mul_f32_e32 v2, v2, v4
	v_mul_f32_e32 v4, v16, v5
	v_mul_f32_e32 v5, v20, v6
	v_mul_f32_e32 v6, v17, v7
	s_waitcnt vmcnt(0)
	v_mul_f32_e32 v7, v21, v8
	v_mul_f32_e32 v8, v18, v9
	v_mul_f32_e32 v9, v22, v10
	v_mul_f32_e32 v10, v19, v11
	v_cvt_pk_bf16_f32 v116, v2, v4
	v_cvt_pk_bf16_f32 v117, v5, v6
	v_cvt_pk_bf16_f32 v118, v7, v8
	v_cvt_pk_bf16_f32 v119, v9, v10
	global_load_dwordx4 v[4:7], v[136:137], off offset:320
	global_load_dwordx4 v[8:11], v[136:137], off offset:336
	v_mul_f32_e32 v2, v83, v64
	v_mul_f32_e32 v16, v83, v65
	v_mul_f32_e32 v17, v83, v66
	v_mul_f32_e32 v18, v83, v67
	s_waitcnt vmcnt(1)
	v_mul_f32_e32 v2, v2, v4
	v_mul_f32_e32 v4, v12, v5
	v_mul_f32_e32 v5, v16, v6
	v_mul_f32_e32 v6, v13, v7
	s_waitcnt vmcnt(0)
	v_mul_f32_e32 v7, v17, v8
	v_mul_f32_e32 v8, v14, v9
	v_mul_f32_e32 v9, v18, v10
	v_mul_f32_e32 v10, v15, v11
	v_cvt_pk_bf16_f32 v120, v2, v4
	v_cvt_pk_bf16_f32 v121, v5, v6
	v_cvt_pk_bf16_f32 v122, v7, v8
	v_cvt_pk_bf16_f32 v123, v9, v10
	global_load_dwordx4 v[4:7], v[136:137], off offset:384
	global_load_dwordx4 v[8:11], v[136:137], off offset:400
	v_mul_f32_e32 v2, v83, v68
	v_mul_f32_e32 v12, v83, v69
	v_mul_f32_e32 v13, v83, v62
	v_mul_f32_e32 v14, v83, v70
	v_mul_f32_e32 v15, v83, v71
	v_mul_f32_e32 v16, v83, v72
	v_mul_f32_e32 v17, v83, v73
	v_mul_f32_e32 v18, v83, v74
	s_waitcnt vmcnt(1)
	v_mul_f32_e32 v2, v2, v4
	v_mul_f32_e32 v4, v12, v5
	v_mul_f32_e32 v5, v13, v6
	v_mul_f32_e32 v6, v14, v7
	s_waitcnt vmcnt(0)
	v_mul_f32_e32 v7, v15, v8
	v_mul_f32_e32 v8, v16, v9
	v_mul_f32_e32 v9, v17, v10
	v_mul_f32_e32 v10, v18, v11
	v_cvt_pk_bf16_f32 v124, v2, v4
	v_cvt_pk_bf16_f32 v125, v5, v6
	v_cvt_pk_bf16_f32 v126, v7, v8
	v_cvt_pk_bf16_f32 v127, v9, v10
	global_load_dwordx4 v[4:7], v[136:137], off offset:448
	global_load_dwordx4 v[8:11], v[136:137], off offset:464
	v_mul_f32_e32 v2, v83, v75
	v_mul_f32_e32 v12, v83, v76
	v_mul_f32_e32 v13, v83, v77
	v_mul_f32_e32 v14, v83, v78
	v_mul_f32_e32 v15, v83, v79
	v_mul_f32_e32 v16, v83, v80
	v_mul_f32_e32 v17, v83, v81
	v_mul_f32_e32 v18, v83, v82
	s_waitcnt vmcnt(1)
	v_mul_f32_e32 v2, v2, v4
	v_mul_f32_e32 v4, v12, v5
	v_mul_f32_e32 v5, v13, v6
	v_mul_f32_e32 v6, v14, v7
	s_waitcnt vmcnt(0)
	v_mul_f32_e32 v7, v15, v8
	v_mul_f32_e32 v8, v16, v9
	v_mul_f32_e32 v9, v17, v10
	v_mul_f32_e32 v10, v18, v11
	v_cvt_pk_bf16_f32 v128, v2, v4
	v_cvt_pk_bf16_f32 v129, v5, v6
	v_cvt_pk_bf16_f32 v130, v7, v8
	v_cvt_pk_bf16_f32 v131, v9, v10
	s_cbranch_vccnz .LBB0_1425
	s_and_b64 vcc, exec, s[6:7]
	s_cbranch_vccnz .LBB0_1425
	v_readlane_b32 s18, v252, 24
	v_readlane_b32 s19, v252, 25
	s_mov_b32 s11, m0
	s_mov_b32 m0, s81
	s_nop 0
	global_load_lds_dword v175, s[18:19]
	s_mov_b32 m0, s11
